# sel block pairing: proposal window widened from +-8 to +-16 list positions and four rounds instead of three, to lower the per-triple maximum wave load
# baseline (speedup 1.0000x reference)
; #define LAS __attribute__((address_space(3)))
; template <bool DUMMY> __device__ __forceinline__ void sel_phase(Frame& F) {
;     const bf16* Q = (const bf16*)(F.ws + SC_Q); const char* KS = (const char*)(F.ws + SC_KV + 2 * KVS);        const char* VS = (const char*)(F.ws + SC_KV + 1 * KVS);
;     bf16* OW = (bf16*)(F.ws + SC_OW); const float* gates = (const float*)(F.ws + SM_GATES); const unsigned long long* SELM = (const unsigned long long*)(F.ws + SM_SELM);
;     const int lane = F.lane, c = lane & 15, kq = lane >> 4;
;     LAS unsigned long long* Ml = (LAS unsigned long long*)(F.lds + RING_ML_OFF);
;     LAS unsigned short* Lst = (LAS unsigned short*)(F.lds + RING_LIST_OFF); LAS unsigned* Wc = (LAS unsigned*)(F.lds + RING_LIST_OFF + 512);
;     LAS u32x2* PD = (LAS u32x2*)(F.lds + 6 * SLOTS);
;     const int vtlane = c * VT8ST + 8 * kq; const int klane = c * K8ST + 32 * kq;
;     RingSLane RL; ringS_lane_init(RL, F.wave, lane);
;     ...
;             const int ia = F.tid >> 2, sub = F.tid & 3;
; #pragma unroll 1
;             for (int r = 0; r < 3 && nB > 0; ++r) {
;                 if (F.tid < 128) PRP[F.tid] = 0xffffffffu;
;                 __syncthreads();
;                 const bool va = ia < npair && PB[ia] == (unsigned short)0xffffu; unsigned best = 0xffffffffu;
;                 if (va) { const unsigned pa = PW[ia]; const int klo = ia - 8 > 0 ? ia - 8 : 0, khi = ia + 8 < nB - 1 ? ia + 8 : nB - 1;
;                     for (int k = klo + sub; k <= khi; k += 4) if (MB[k] == 0) { const unsigned x = pa + PW[npair + k];
.LBB0_1699:
	s_cmpk_gt_i32 s77, 0x7ff
	s_cbranch_scc1 .LBB0_1817
	s_add_u32 s22, s28, 0x1a000000
	s_addc_u32 s23, s29, 0
	s_add_u32 s78, s28, 0x26000000
	s_addc_u32 s79, s29, 0
	s_add_u32 s80, s28, 0x24000000
	s_addc_u32 s81, s29, 0
	s_add_u32 s24, s28, 0x2e000000
	v_writelane_b32 v238, s90, 7
	s_addc_u32 s25, s29, 0
	v_add_u32_e32 v0, s8, v0
	v_writelane_b32 v238, s92, 3
	s_add_u32 s42, s28, 0xe40000
	v_add_u32_e32 v0, 0x4000, v0
	s_mov_b32 s2, 0x66666667
	v_writelane_b32 v238, s93, 4
	s_addc_u32 s43, s29, 0
	v_mul_hi_i32 v1, v0, s2
	s_lshl_b32 s83, s96, 3
	v_writelane_b32 v238, s94, 5
	v_lshrrev_b32_e32 v9, 31, v1
	v_ashrrev_i32_e32 v1, 5, v1
	s_cmpk_gt_u32 s21, 0xff
	v_writelane_b32 v238, s95, 6
	v_add_u32_e32 v1, v1, v9
	s_movk_i32 s10, 0x50
	s_cselect_b64 s[4:5], -1, 0
	v_min_i32_e32 v9, 0x7f, v1
	v_mul_lo_u32 v1, v1, s10
	v_writelane_b32 v238, s4, 8
	s_cmpk_lt_u32 s21, 0x100
	v_sub_u32_e32 v0, v0, v1
	v_cmp_eq_u32_e32 vcc, 0, v2
	v_writelane_b32 v238, s5, 9
	s_cselect_b64 s[4:5], -1, 0
	v_ashrrev_i32_e32 v0, 4, v0
	s_and_b64 s[46:47], s[4:5], vcc
	v_lshlrev_b32_e32 v9, 6, v9
	v_min_i32_e32 v0, 3, v0
	s_bitcmp1_b32 s21, 6
	v_lshl_add_u32 v108, v0, 4, v9
	v_lshlrev_b64 v[0:1], v2, -1
	s_cselect_b64 s[48:49], -1, 0
	s_add_i32 s84, s83, 0
	v_not_b32_e32 v110, v0
	s_movk_i32 s6, 0x80
	v_and_b32_e32 v0, 0xffffff80, v100
	s_add_i32 s84, s84, 0x1c800
	s_add_i32 s85, s8, 0
	v_ashrrev_i32_e32 v101, 31, v100
	v_not_b32_e32 v111, v1
	v_cmp_gt_i32_e64 s[4:5], s6, v100
	v_cmp_eq_u32_e64 s[6:7], s6, v0
	s_cmpk_lt_u32 s21, 0xc0
	v_lshl_add_u64 v[0:1], v[100:101], 3, s[28:29]
	s_mov_b64 s[8:9], 0x1450000
	s_cselect_b64 s[50:51], -1, 0
	v_lshl_add_u64 v[112:113], v[0:1], 0, s[8:9]
	s_add_i32 s8, 0, 0x23000
	v_lshl_add_u32 v101, v100, 3, s8
	s_lshl_b32 s8, s96, 2
	s_add_i32 s88, s8, 0
	v_lshlrev_b32_e32 v0, 1, v100
	s_add_i32 s8, 0, 0x23800
	v_add_u32_e32 v157, s8, v0
	v_lshlrev_b32_e32 v1, 2, v100
	s_add_i32 s8, 0, 0x1a400
	s_add_i32 s12, 0, 0x1a800
	v_ashrrev_i32_e32 v156, 2, v100
	v_add_u32_e32 v158, s8, v1
	s_add_i32 s11, 0, 0x1aa00
	v_add_u32_e32 v165, s12, v1
	v_and_b32_e32 v1, 0x7f, v100
	v_add_u32_e32 v159, s11, v0
	v_lshl_add_u32 v160, v156, 1, s11
	v_lshl_add_u32 v166, v1, 1, s11
	s_add_i32 s11, 0, 0x1ab80
	s_add_i32 s21, s88, 0x23a00
	s_add_i32 s87, s88, 0x1ac80
	s_add_i32 s88, s88, 0x1ac7c
	v_add_u32_e32 v169, s11, v0
	s_add_i32 s11, 0, 0x1ac90
	s_add_u32 s52, s28, 0x3b400000
	v_add_u32_e32 v170, s11, v0
	s_addc_u32 s53, s29, 0
	s_add_i32 s11, s96, -4
	s_lshr_b32 s12, s11, 2
	s_add_i32 s12, s12, 1
	s_and_b32 s34, s96, 0x3fffffc
	s_and_b32 s13, s12, 7
	s_cmp_gt_u32 s11, 27
	s_cselect_b64 s[36:37], -1, 0
	v_writelane_b32 v238, s36, 10
	s_and_b32 s11, s12, 0x7ffffff8
	s_cmp_lg_u32 s13, 0
	v_writelane_b32 v238, s37, 11
	v_writelane_b32 v238, s11, 12
	s_cselect_b64 s[36:37], -1, 0
	v_writelane_b32 v238, s36, 13
	s_cmp_lg_u32 s96, s34
	v_lshl_add_u32 v102, v3, 4, v4
	v_writelane_b32 v238, s37, 14
	v_ashrrev_i32_e32 v4, 4, v2
	v_writelane_b32 v238, s34, 15
	s_cselect_b64 s[34:35], -1, 0
	v_lshlrev_b32_e32 v7, 3, v4
	v_lshlrev_b32_e32 v104, 5, v4
	v_lshlrev_b32_e32 v155, 2, v4
	v_and_b32_e32 v4, -4, v100
	v_writelane_b32 v238, s34, 16
	v_and_b32_e32 v3, 15, v2
	v_and_b32_e32 v153, 3, v2
	v_add_u32_e32 v161, s8, v4
	v_max_i32_e32 v4, 16, v156
	v_writelane_b32 v238, s35, 17
	s_lshl_b32 s11, s13, 4
	v_lshlrev_b32_e32 v0, 3, v2
	v_mul_u32_u24_e32 v8, 0x90, v3
	v_bfe_u32 v152, v2, 2, 2
	v_mov_b32_e32 v17, 0
	s_movk_i32 s2, 0x100
	v_add_u32_e32 v163, v4, v153
	v_writelane_b32 v238, s11, 18
	v_lshl_add_u32 v172, s96, 9, v0
	v_mad_u32_u24 v0, v3, s10, 0
	s_movk_i32 s10, 0x2400
	v_lshl_add_u32 v106, v5, 4, v6
	v_ashrrev_i32_e32 v105, 31, v104
	s_mov_b32 s82, 0
	v_mov_b32_e32 v103, v17
	v_mov_b32_e32 v107, v17
	v_mov_b32_e32 v109, v17
	v_lshlrev_b32_e64 v154, v152, 1
	v_cmp_gt_i32_e64 s[2:3], s2, v100
	s_movk_i32 s86, 0xc0
	v_add_u32_e32 v162, 16, v156
	v_add_u32_e32 v164, -16, v163
	v_cmp_eq_u32_e64 s[8:9], 0, v153
	v_add_u32_e32 v167, 0xffffff80, v100
	v_add_u16_e32 v168, 0xff80, v100
	v_sub_u32_e32 v171, 0, v156
	v_writelane_b32 v238, s96, 19
	v_add3_u32 v173, v0, v7, s10
	v_add_u32_e32 v173, v173, v7
	v_add3_u32 v174, v8, 0, v104
	v_mov_b32_e32 v175, -1
	v_mov_b32_e32 v176, 1
	s_add_i32 s92, 0, 0x1ac88
	s_mov_b32 s93, 0xffff
	s_add_i32 s94, s85, 0x2000
	s_add_i32 s95, s85, 0x4c00
	s_add_i32 s96, s85, 0x6c00
	s_add_i32 s10, s85, 0x8c00
	s_add_i32 s34, s85, 0x9800
	s_add_i32 s35, s85, 0xb800
	s_add_i32 s75, s85, 0xd800
	s_mov_b32 s90, 0xefa18f08
	v_mov_b32_e32 v177, 0x7c7c7c7c
	v_mov_b32_e32 v178, 0x7f7f7f7f
	s_brev_b32 s91, -3
	v_mov_b32_e32 v115, 0x40400000
	v_mov_b32_e32 v179, 0x1a3e0
	v_mov_b32_e32 v180, 0x1000000
	v_mov_b32_e32 v181, 0xff800000
	s_mov_b32 s74, s77
	v_writelane_b32 v238, s10, 20
	s_branch .LBB0_1703

; template <bool DUMMY> __device__ __forceinline__ void sel_phase(Frame& F) {
;     ...
;             for (int r = 0; r < 3 && nB > 0; ++r) {
;                 if (F.tid < 128) PRP[F.tid] = 0xffffffffu;
;                 __syncthreads();
;                 const bool va = ia < npair && PB[ia] == (unsigned short)0xffffu; unsigned best = 0xffffffffu;
;                 if (va) { const unsigned pa = PW[ia]; const int klo = ia - 8 > 0 ? ia - 8 : 0, khi = ia + 8 < nB - 1 ? ia + 8 : nB - 1;
;                     for (int k = klo + sub; k <= khi; k += 4) if (MB[k] == 0) { const unsigned x = pa + PW[npair + k];
;                         const unsigned cst = (x != 0u) + (((x + 0x66666666u) & 0x88888888u) != 0u) + (((x + 0x55555555u) & 0x88888888u) != 0u) + (((x + 0x44444444u) & 0x88888888u) != 0u);
;                         const int dist = k > ia ? k - ia : ia - k;
;                         const unsigned key = (cst << 24) | ((unsigned)dist << 8) | (unsigned)k; best = key < best ? key : best; } }
;                 { const unsigned o1 = (unsigned)__builtin_amdgcn_mov_dpp((int)best, 0xB1, 0xF, 0xF, true); best = o1 < best ? o1 : best; const unsigned o2 = (unsigned)__builtin_amdgcn_mov_dpp((int)best, 0x4E, 0xF, 0xF, true); best = o2 < best ? o2 : best; }
;                 const bool prop = va && sub == 0 && best != 0xffffffffu; const unsigned kb_ = best & 0xffu, myp = ((best >> 24) << 16) | (unsigned)ia;
;                 if (prop) __hip_atomic_fetch_min(PRP + kb_, myp, __ATOMIC_RELAXED, __HIP_MEMORY_SCOPE_WORKGROUP);
;                 __syncthreads();
;                 if (prop && PRP[kb_] == myp) { PB[ia] = (unsigned short)(npair + kb_); MB[kb_] = 1; }
;                 __syncthreads();
.LBB0_1728:
	s_or_b64 exec, exec, s[64:65]
	s_add_i32 s45, s45, 1
	s_cmp_eq_u32 s45, 4
	s_waitcnt lgkmcnt(0)
	s_barrier
	s_cbranch_scc1 .LBB0_1746
